# s11p + mLSTM chunk-local unit: 4 tile loads and the 4-trip scaled fill loop issue all 8 loads up front, LDS writes behind counted vmcnt (L0 and L1); padded
# baseline (speedup 1.0000x reference)
; #define LAS __attribute__((address_space(3)))
; DI unsigned pk2(float lo, float hi) { const f32x2 v = {lo, hi}; return __builtin_bit_cast(unsigned, __builtin_convertvector(v, bf16x2_t)); }
; DI float wave_max(float v) { v = fmaxf(v, shx<1>(v)); v = fmaxf(v, shx<2>(v)); v = fmaxf(v, shx<4>(v)); v = fmaxf(v, shx<8>(v)); v = fmaxf(v, shx<16>(v)); v = fmaxf(v, shx<32>(v)); return v; }
; template <int NW> DI void ml1_unit(const Params& P, const Frame& F, int cidx) {
;     ...
;       if (F.tid < 64) { const float lf = GD[(r0 + F.tid) * 16 + 12 + h], ip = GD[(r0 + F.tid) * 16 + 8 + h]; const float e = ip - wave_incl_sum(lf, lane); wl[F.tid] = __expf(e - wave_max(e)); } }
;     __syncthreads();
;     for (int id = F.tid; id < 2048; id += NT) { const int which = id >> 10, rem = id & 1023, row = rem >> 4, ch = rem & 15;
;         if (which == 0) *(LAS u32x4*)(Vs + row * 272 + ch * 16) = *(const u32x4*)(Z + (r0 + row) * NZ + 6144 + h * 128 + ch * 8);
;         else { const u32x4 k = *(const u32x4*)(ZC + (r0 + row) * 2560 + 2048 + h * 128 + ch * 8); const float w = wl[row];
;             u32x4 o; o.x = pk2(bflo(k.x) * w, bfhi(k.x) * w); o.y = pk2(bflo(k.y) * w, bfhi(k.y) * w); o.z = pk2(bflo(k.z) * w, bfhi(k.z) * w); o.w = pk2(bflo(k.w) * w, bfhi(k.w) * w);
;             *(LAS u32x4*)(KWs + row * 272 + ch * 16) = o; } }
.LBB0_968:
	s_or_b64 exec, exec, s[20:21]
	s_lshl_b32 s0, s29, 8
	v_lshl_add_u64 v[0:1], v[16:17], 0, s[0:1]
	s_waitcnt lgkmcnt(0)
	s_barrier
	global_load_dwordx4 v[186:189], v[0:1], off
	v_lshl_add_u64 v[2:3], v[18:19], 0, s[0:1]
	global_load_dwordx4 v[190:193], v[2:3], off
	v_lshl_add_u64 v[0:1], v[20:21], 0, s[0:1]
	global_load_dwordx4 v[194:197], v[0:1], off
	v_lshl_add_u64 v[2:3], v[22:23], 0, s[0:1]
	global_load_dwordx4 v[198:201], v[2:3], off
	s_add_i32 s0, s33, s25
	s_and_b32 s0, s0, 3
	s_lshl_b32 s0, s0, 8
	s_xor_b64 s[20:21], s[22:23], -1
	s_mov_b64 s[30:31], 0x14000
	v_lshl_add_u64 v[0:1], v[58:59], 0, s[0:1]
	global_load_dwordx4 v[202:205], v[0:1], off
	v_lshl_add_u64 v[0:1], v[0:1], 0, s[30:31]
	global_load_dwordx4 v[206:209], v[0:1], off
	v_lshl_add_u64 v[0:1], v[0:1], 0, s[30:31]
	global_load_dwordx4 v[210:213], v[0:1], off
	v_lshl_add_u64 v[0:1], v[0:1], 0, s[30:31]
	global_load_dwordx4 v[214:217], v[0:1], off
	ds_read_b32 v230, v69
	ds_read_b32 v232, v69 offset:64
	ds_read_b32 v234, v69 offset:128
	ds_read_b32 v236, v69 offset:192
	v_mad_u32_u24 v244, v56, s26, v114
	v_add_u32_e32 v3, 16, v56
	v_mad_u32_u24 v245, v3, s26, v114
	v_add_u32_e32 v3, 32, v56
	v_mad_u32_u24 v246, v3, s26, v114
	v_add_u32_e32 v3, 48, v56
	v_mad_u32_u24 v247, v3, s26, v114
	s_waitcnt vmcnt(7)
	ds_write_b128 v57, v[186:189]
	s_waitcnt vmcnt(6)
	ds_write_b128 v57, v[190:193] offset:4352
	s_waitcnt vmcnt(5)
	ds_write_b128 v57, v[194:197] offset:8704
	s_waitcnt vmcnt(4)
	ds_write_b128 v57, v[198:201] offset:13056
	s_waitcnt vmcnt(3)
	s_waitcnt lgkmcnt(4)
	v_lshlrev_b32_e32 v60, 16, v202
	v_and_b32_e32 v61, 0xffff0000, v202
	v_pk_mul_f32 v[60:61], v[230:231], v[60:61] op_sel_hi:[0,1]
	v_cvt_pk_bf16_f32 v202, v60, v61
	v_lshlrev_b32_e32 v60, 16, v203
	v_and_b32_e32 v61, 0xffff0000, v203
	v_pk_mul_f32 v[60:61], v[230:231], v[60:61] op_sel_hi:[0,1]
	v_cvt_pk_bf16_f32 v203, v60, v61
	v_lshlrev_b32_e32 v60, 16, v204
	v_and_b32_e32 v61, 0xffff0000, v204
	v_pk_mul_f32 v[60:61], v[230:231], v[60:61] op_sel_hi:[0,1]
	v_cvt_pk_bf16_f32 v204, v60, v61
	v_lshlrev_b32_e32 v60, 16, v205
	v_and_b32_e32 v61, 0xffff0000, v205
	v_pk_mul_f32 v[60:61], v[230:231], v[60:61] op_sel_hi:[0,1]
	v_cvt_pk_bf16_f32 v205, v60, v61
	ds_write_b128 v244, v[202:205] offset:17408
	s_waitcnt vmcnt(2)
	v_lshlrev_b32_e32 v60, 16, v206
	v_and_b32_e32 v61, 0xffff0000, v206
	v_pk_mul_f32 v[60:61], v[232:233], v[60:61] op_sel_hi:[0,1]
	v_cvt_pk_bf16_f32 v206, v60, v61
	v_lshlrev_b32_e32 v60, 16, v207
	v_and_b32_e32 v61, 0xffff0000, v207
	v_pk_mul_f32 v[60:61], v[232:233], v[60:61] op_sel_hi:[0,1]
	v_cvt_pk_bf16_f32 v207, v60, v61
	v_lshlrev_b32_e32 v60, 16, v208
	v_and_b32_e32 v61, 0xffff0000, v208
	v_pk_mul_f32 v[60:61], v[232:233], v[60:61] op_sel_hi:[0,1]
	v_cvt_pk_bf16_f32 v208, v60, v61
	v_lshlrev_b32_e32 v60, 16, v209
	v_and_b32_e32 v61, 0xffff0000, v209
	v_pk_mul_f32 v[60:61], v[232:233], v[60:61] op_sel_hi:[0,1]
	v_cvt_pk_bf16_f32 v209, v60, v61
	ds_write_b128 v245, v[206:209] offset:17408
	s_waitcnt vmcnt(1)
	v_lshlrev_b32_e32 v60, 16, v210
	v_and_b32_e32 v61, 0xffff0000, v210
	v_pk_mul_f32 v[60:61], v[234:235], v[60:61] op_sel_hi:[0,1]
	v_cvt_pk_bf16_f32 v210, v60, v61
	v_lshlrev_b32_e32 v60, 16, v211
	v_and_b32_e32 v61, 0xffff0000, v211
	v_pk_mul_f32 v[60:61], v[234:235], v[60:61] op_sel_hi:[0,1]
	v_cvt_pk_bf16_f32 v211, v60, v61
	v_lshlrev_b32_e32 v60, 16, v212
	v_and_b32_e32 v61, 0xffff0000, v212
	v_pk_mul_f32 v[60:61], v[234:235], v[60:61] op_sel_hi:[0,1]
	v_cvt_pk_bf16_f32 v212, v60, v61
	v_lshlrev_b32_e32 v60, 16, v213
	v_and_b32_e32 v61, 0xffff0000, v213
	v_pk_mul_f32 v[60:61], v[234:235], v[60:61] op_sel_hi:[0,1]
	v_cvt_pk_bf16_f32 v213, v60, v61
	ds_write_b128 v246, v[210:213] offset:17408
	s_waitcnt vmcnt(0)
	v_lshlrev_b32_e32 v60, 16, v214
	v_and_b32_e32 v61, 0xffff0000, v214
	v_pk_mul_f32 v[60:61], v[236:237], v[60:61] op_sel_hi:[0,1]
	v_cvt_pk_bf16_f32 v214, v60, v61
	v_lshlrev_b32_e32 v60, 16, v215
	v_and_b32_e32 v61, 0xffff0000, v215
	v_pk_mul_f32 v[60:61], v[236:237], v[60:61] op_sel_hi:[0,1]
	v_cvt_pk_bf16_f32 v215, v60, v61
	v_lshlrev_b32_e32 v60, 16, v216
	v_and_b32_e32 v61, 0xffff0000, v216
	v_pk_mul_f32 v[60:61], v[236:237], v[60:61] op_sel_hi:[0,1]
	v_cvt_pk_bf16_f32 v216, v60, v61
	v_lshlrev_b32_e32 v60, 16, v217
	v_and_b32_e32 v61, 0xffff0000, v217
	v_pk_mul_f32 v[60:61], v[236:237], v[60:61] op_sel_hi:[0,1]
	v_cvt_pk_bf16_f32 v217, v60, v61
	ds_write_b128 v247, v[214:217] offset:17408
	s_mov_b64 s[22:23], exec
	s_movk_i32 s0, 0x6ff
	s_or_b64 exec, exec, s[22:23]
	s_waitcnt lgkmcnt(0)
	s_barrier
; DI bf16x8 frag_tr(unsigned base_addr, int RS, int k0, int c0, int lane) { const int g = lane >> 4; return frag_tr2(base_addr, RS, k0 + 8 * g, k0 + 8 * g + 4, c0, lane); }
; #define MFMA16(a, b, c) __builtin_amdgcn_mfma_f32_16x16x32_bf16((a), (b), (c), 0, 0, 0)
; template <int NW> DI void ml1_unit(const Params& P, const Frame& F, int cidx) {
;     ...
;     float* DCT = (float*)(ws + WS_T + T_DCT) + (size_t)cidx * 16512;
;     const unsigned Va = (unsigned)(size_t)Vs, Ka = (unsigned)(size_t)KWs;
; #pragma unroll
;     for (int mi = 0; mi < 8 / NW; ++mi) { const int mt = F.wave + NW * mi;
;         bf16x8 af[2];
; #pragma unroll
;         for (int ks = 0; ks < 2; ++ks) af[ks] = frag_tr(Va, 272, 32 * ks, 16 * mt, lane);
; #pragma unroll
;         for (int nt = 0; nt < 8; ++nt) { f32x4 a = (f32x4){0.f, 0.f, 0.f, 0.f};
; #pragma unroll
;             for (int ks = 0; ks < 2; ++ks) a = MFMA16(af[ks], frag_tr(Ka, 272, 32 * ks, 16 * nt, lane), a);
; #pragma unroll
;             for (int e = 0; e < 4; ++e) DCT[(16 * mt + 4 * rq + e) * 128 + 16 * nt + c] = a[e]; } }
	ds_read_b64_tr_b16 v[4:5], v70
	ds_read_b64_tr_b16 v[6:7], v71
	s_waitcnt lgkmcnt(0)
	ds_read_b64_tr_b16 v[0:1], v74
	ds_read_b64_tr_b16 v[2:3], v75
	s_waitcnt lgkmcnt(0)
	ds_read_b64_tr_b16 v[116:117], v76
	ds_read_b64_tr_b16 v[118:119], v78
	s_waitcnt lgkmcnt(0)
	s_lshl_b32 s0, s24, 5
	v_mfma_f32_16x16x32_bf16 v[116:119], v[4:7], v[116:119], 0
	s_or_b32 s0, s0, s93
	s_mul_hi_i32 s23, s0, 0x10200
	s_mul_i32 s0, s0, 0x10200
	ds_read_b64_tr_b16 v[120:121], v79
	ds_read_b64_tr_b16 v[122:123], v80
	s_waitcnt lgkmcnt(0)
	s_add_u32 s22, s27, s0
	v_mfma_f32_16x16x32_bf16 v[116:119], v[0:3], v[120:123], v[116:119]
	s_addc_u32 s23, s28, s23
	v_lshl_add_u64 v[60:61], v[14:15], 2, s[22:23]
	s_nop 5
	global_store_dword v[60:61], v116, off
	v_lshl_add_u64 v[60:61], v[24:25], 2, s[22:23]
	global_store_dword v[60:61], v117, off offset:512
	global_store_dword v[60:61], v118, off offset:1024
	global_store_dword v[60:61], v119, off offset:1536
	ds_read_b64_tr_b16 v[116:117], v81
	ds_read_b64_tr_b16 v[118:119], v82
	s_waitcnt lgkmcnt(0)
	ds_read_b64_tr_b16 v[120:121], v83
	ds_read_b64_tr_b16 v[122:123], v84
	s_waitcnt lgkmcnt(0)
	s_nop 0
	v_mfma_f32_16x16x32_bf16 v[116:119], v[4:7], v[116:119], 0
	v_mfma_f32_16x16x32_bf16 v[116:119], v[0:3], v[120:123], v[116:119]
	v_lshl_add_u64 v[120:121], v[26:27], 2, s[22:23]
	s_nop 6
	global_store_dword v[60:61], v116, off offset:64
	global_store_dword v[120:121], v117, off offset:512
	global_store_dword v[120:121], v118, off offset:1024
	global_store_dword v[120:121], v119, off offset:1536
	ds_read_b64_tr_b16 v[116:117], v85
	ds_read_b64_tr_b16 v[118:119], v86
	s_waitcnt lgkmcnt(0)
	ds_read_b64_tr_b16 v[120:121], v87
	ds_read_b64_tr_b16 v[122:123], v88
	s_waitcnt lgkmcnt(0)
	s_nop 0
	v_mfma_f32_16x16x32_bf16 v[116:119], v[4:7], v[116:119], 0
	v_mfma_f32_16x16x32_bf16 v[116:119], v[0:3], v[120:123], v[116:119]
	v_lshl_add_u64 v[120:121], v[28:29], 2, s[22:23]
	s_nop 6
	global_store_dword v[60:61], v116, off offset:128
	global_store_dword v[120:121], v117, off offset:512
	global_store_dword v[120:121], v118, off offset:1024
	global_store_dword v[120:121], v119, off offset:1536
	ds_read_b64_tr_b16 v[116:117], v89
	ds_read_b64_tr_b16 v[118:119], v90
	s_waitcnt lgkmcnt(0)
	ds_read_b64_tr_b16 v[120:121], v91
	ds_read_b64_tr_b16 v[122:123], v92
	s_waitcnt lgkmcnt(0)
	s_nop 0
	v_mfma_f32_16x16x32_bf16 v[116:119], v[4:7], v[116:119], 0
	v_mfma_f32_16x16x32_bf16 v[116:119], v[0:3], v[120:123], v[116:119]
	v_lshl_add_u64 v[120:121], v[30:31], 2, s[22:23]
	s_nop 6
	global_store_dword v[60:61], v116, off offset:192
	global_store_dword v[120:121], v117, off offset:512
	global_store_dword v[120:121], v118, off offset:1024
	global_store_dword v[120:121], v119, off offset:1536
	ds_read_b64_tr_b16 v[116:117], v93
	ds_read_b64_tr_b16 v[118:119], v94
	s_waitcnt lgkmcnt(0)
	ds_read_b64_tr_b16 v[120:121], v95
	ds_read_b64_tr_b16 v[122:123], v96
	s_waitcnt lgkmcnt(0)
	s_nop 0
	v_mfma_f32_16x16x32_bf16 v[116:119], v[4:7], v[116:119], 0
	v_mfma_f32_16x16x32_bf16 v[116:119], v[0:3], v[120:123], v[116:119]
	v_lshl_add_u64 v[120:121], v[32:33], 2, s[22:23]
	s_nop 6
	global_store_dword v[60:61], v116, off offset:256
	global_store_dword v[120:121], v117, off offset:512
	global_store_dword v[120:121], v118, off offset:1024
	global_store_dword v[120:121], v119, off offset:1536
	ds_read_b64_tr_b16 v[116:117], v97
	ds_read_b64_tr_b16 v[118:119], v98
	s_waitcnt lgkmcnt(0)
	ds_read_b64_tr_b16 v[120:121], v99
	ds_read_b64_tr_b16 v[122:123], v100
	s_waitcnt lgkmcnt(0)
	s_nop 0
	v_mfma_f32_16x16x32_bf16 v[116:119], v[4:7], v[116:119], 0
	v_mfma_f32_16x16x32_bf16 v[116:119], v[0:3], v[120:123], v[116:119]
	v_lshl_add_u64 v[120:121], v[34:35], 2, s[22:23]
	s_nop 6
	global_store_dword v[60:61], v116, off offset:320
	global_store_dword v[120:121], v117, off offset:512
	global_store_dword v[120:121], v118, off offset:1024
	global_store_dword v[120:121], v119, off offset:1536
	ds_read_b64_tr_b16 v[116:117], v101
	ds_read_b64_tr_b16 v[118:119], v102
	s_waitcnt lgkmcnt(0)
	ds_read_b64_tr_b16 v[120:121], v103
	ds_read_b64_tr_b16 v[122:123], v104
	s_waitcnt lgkmcnt(0)
	s_nop 0
	v_mfma_f32_16x16x32_bf16 v[116:119], v[4:7], v[116:119], 0
	v_mfma_f32_16x16x32_bf16 v[116:119], v[0:3], v[120:123], v[116:119]
	v_lshl_add_u64 v[120:121], v[36:37], 2, s[22:23]
	s_nop 6
	global_store_dword v[60:61], v116, off offset:384
	global_store_dword v[120:121], v117, off offset:512
	global_store_dword v[120:121], v118, off offset:1024
	global_store_dword v[120:121], v119, off offset:1536
	ds_read_b64_tr_b16 v[116:117], v105
	ds_read_b64_tr_b16 v[118:119], v106
	s_waitcnt lgkmcnt(0)
	s_nop 0
	v_mfma_f32_16x16x32_bf16 v[4:7], v[4:7], v[116:119], 0
	ds_read_b64_tr_b16 v[116:117], v107
	ds_read_b64_tr_b16 v[118:119], v108
	s_waitcnt lgkmcnt(0)
	s_nop 0
	v_mfma_f32_16x16x32_bf16 v[0:3], v[0:3], v[116:119], v[4:7]
	s_nop 5
	v_lshl_add_u64 v[4:5], v[38:39], 2, s[22:23]
	s_nop 0
	global_store_dword v[60:61], v0, off offset:448
	global_store_dword v[4:5], v1, off offset:512
	global_store_dword v[4:5], v2, off offset:1024
	global_store_dword v[4:5], v3, off offset:1536
	ds_read_b64_tr_b16 v[4:5], v109
	ds_read_b64_tr_b16 v[6:7], v110
	s_waitcnt lgkmcnt(0)
	ds_read_b64_tr_b16 v[0:1], v111
	ds_read_b64_tr_b16 v[2:3], v112
	s_waitcnt lgkmcnt(0)
	ds_read_b64_tr_b16 v[116:117], v76
	ds_read_b64_tr_b16 v[118:119], v78
	s_waitcnt lgkmcnt(0)
	ds_read_b64_tr_b16 v[120:121], v79
	ds_read_b64_tr_b16 v[122:123], v80
	s_waitcnt lgkmcnt(0)
; #define LAS __attribute__((address_space(3)))
; DI bf16x8 frag_tr(unsigned base_addr, int RS, int k0, int c0, int lane) { const int g = lane >> 4; return frag_tr2(base_addr, RS, k0 + 8 * g, k0 + 8 * g + 4, c0, lane); }
; #define MFMA16(a, b, c) __builtin_amdgcn_mfma_f32_16x16x32_bf16((a), (b), (c), 0, 0, 0)
; template <int NW> DI void ml1_unit(const Params& P, const Frame& F, int cidx) {
;     ...
; #pragma unroll
;     for (int mi = 0; mi < 8 / NW; ++mi) { const int mt = F.wave + NW * mi;
;         bf16x8 af[2];
; #pragma unroll
;         for (int ks = 0; ks < 2; ++ks) af[ks] = frag_tr(Va, 272, 32 * ks, 16 * mt, lane);
; #pragma unroll
;         for (int nt = 0; nt < 8; ++nt) { f32x4 a = (f32x4){0.f, 0.f, 0.f, 0.f};
; #pragma unroll
;             for (int ks = 0; ks < 2; ++ks) a = MFMA16(af[ks], frag_tr(Ka, 272, 32 * ks, 16 * nt, lane), a);
; #pragma unroll
;             for (int e = 0; e < 4; ++e) DCT[(16 * mt + 4 * rq + e) * 128 + 16 * nt + c] = a[e]; } }
;     if (F.tid < 128) { float s = 0.f; for (int j = 0; j < 64; ++j) s += bf2f(*(const LAS bf16*)(KWs + j * 272 + F.tid * 2)); DCT[128 * 128 + F.tid] = s; }
	v_lshl_add_u64 v[60:61], v[12:13], 2, s[22:23]
	v_mfma_f32_16x16x32_bf16 v[116:119], v[4:7], v[116:119], 0
	v_mfma_f32_16x16x32_bf16 v[116:119], v[0:3], v[120:123], v[116:119]
	s_nop 7
	global_store_dword v[60:61], v116, off
	v_lshl_add_u64 v[60:61], v[40:41], 2, s[22:23]
	global_store_dword v[60:61], v117, off offset:512
	global_store_dword v[60:61], v118, off offset:1024
	global_store_dword v[60:61], v119, off offset:1536
	ds_read_b64_tr_b16 v[116:117], v81
	ds_read_b64_tr_b16 v[118:119], v82
	s_waitcnt lgkmcnt(0)
	ds_read_b64_tr_b16 v[120:121], v83
	ds_read_b64_tr_b16 v[122:123], v84
	s_waitcnt lgkmcnt(0)
	s_nop 0
	v_mfma_f32_16x16x32_bf16 v[116:119], v[4:7], v[116:119], 0
	v_mfma_f32_16x16x32_bf16 v[116:119], v[0:3], v[120:123], v[116:119]
	v_lshl_add_u64 v[120:121], v[42:43], 2, s[22:23]
	s_nop 6
	global_store_dword v[60:61], v116, off offset:64
	global_store_dword v[120:121], v117, off offset:512
	global_store_dword v[120:121], v118, off offset:1024
	global_store_dword v[120:121], v119, off offset:1536
	ds_read_b64_tr_b16 v[116:117], v85
	ds_read_b64_tr_b16 v[118:119], v86
	s_waitcnt lgkmcnt(0)
	ds_read_b64_tr_b16 v[120:121], v87
	ds_read_b64_tr_b16 v[122:123], v88
	s_waitcnt lgkmcnt(0)
	s_nop 0
	v_mfma_f32_16x16x32_bf16 v[116:119], v[4:7], v[116:119], 0
	v_mfma_f32_16x16x32_bf16 v[116:119], v[0:3], v[120:123], v[116:119]
	v_lshl_add_u64 v[120:121], v[44:45], 2, s[22:23]
	s_nop 6
	global_store_dword v[60:61], v116, off offset:128
	global_store_dword v[120:121], v117, off offset:512
	global_store_dword v[120:121], v118, off offset:1024
	global_store_dword v[120:121], v119, off offset:1536
	ds_read_b64_tr_b16 v[116:117], v89
	ds_read_b64_tr_b16 v[118:119], v90
	s_waitcnt lgkmcnt(0)
	ds_read_b64_tr_b16 v[120:121], v91
	ds_read_b64_tr_b16 v[122:123], v92
	s_waitcnt lgkmcnt(0)
	s_nop 0
	v_mfma_f32_16x16x32_bf16 v[116:119], v[4:7], v[116:119], 0
	v_mfma_f32_16x16x32_bf16 v[116:119], v[0:3], v[120:123], v[116:119]
	v_lshl_add_u64 v[120:121], v[46:47], 2, s[22:23]
	s_nop 6
	global_store_dword v[60:61], v116, off offset:192
	global_store_dword v[120:121], v117, off offset:512
	global_store_dword v[120:121], v118, off offset:1024
	global_store_dword v[120:121], v119, off offset:1536
	ds_read_b64_tr_b16 v[116:117], v93
	ds_read_b64_tr_b16 v[118:119], v94
	s_waitcnt lgkmcnt(0)
	ds_read_b64_tr_b16 v[120:121], v95
	ds_read_b64_tr_b16 v[122:123], v96
	s_waitcnt lgkmcnt(0)
	s_nop 0
	v_mfma_f32_16x16x32_bf16 v[116:119], v[4:7], v[116:119], 0
	v_mfma_f32_16x16x32_bf16 v[116:119], v[0:3], v[120:123], v[116:119]
	v_lshl_add_u64 v[120:121], v[48:49], 2, s[22:23]
	s_nop 6
	global_store_dword v[60:61], v116, off offset:256
	global_store_dword v[120:121], v117, off offset:512
	global_store_dword v[120:121], v118, off offset:1024
	global_store_dword v[120:121], v119, off offset:1536
	ds_read_b64_tr_b16 v[116:117], v97
	ds_read_b64_tr_b16 v[118:119], v98
	s_waitcnt lgkmcnt(0)
	ds_read_b64_tr_b16 v[120:121], v99
	ds_read_b64_tr_b16 v[122:123], v100
	s_waitcnt lgkmcnt(0)
	s_nop 0
	v_mfma_f32_16x16x32_bf16 v[116:119], v[4:7], v[116:119], 0
	v_mfma_f32_16x16x32_bf16 v[116:119], v[0:3], v[120:123], v[116:119]
	v_lshl_add_u64 v[120:121], v[50:51], 2, s[22:23]
	s_nop 6
	global_store_dword v[60:61], v116, off offset:320
	global_store_dword v[120:121], v117, off offset:512
	global_store_dword v[120:121], v118, off offset:1024
	global_store_dword v[120:121], v119, off offset:1536
	ds_read_b64_tr_b16 v[116:117], v101
	ds_read_b64_tr_b16 v[118:119], v102
	s_waitcnt lgkmcnt(0)
	ds_read_b64_tr_b16 v[120:121], v103
	ds_read_b64_tr_b16 v[122:123], v104
	s_waitcnt lgkmcnt(0)
	s_nop 0
	v_mfma_f32_16x16x32_bf16 v[116:119], v[4:7], v[116:119], 0
	v_mfma_f32_16x16x32_bf16 v[116:119], v[0:3], v[120:123], v[116:119]
	v_lshl_add_u64 v[120:121], v[52:53], 2, s[22:23]
	s_nop 6
	global_store_dword v[60:61], v116, off offset:384
	global_store_dword v[120:121], v117, off offset:512
	global_store_dword v[120:121], v118, off offset:1024
	global_store_dword v[120:121], v119, off offset:1536
	ds_read_b64_tr_b16 v[116:117], v105
	ds_read_b64_tr_b16 v[118:119], v106
	s_waitcnt lgkmcnt(0)
	s_nop 0
	v_mfma_f32_16x16x32_bf16 v[4:7], v[4:7], v[116:119], 0
	ds_read_b64_tr_b16 v[116:117], v107
	ds_read_b64_tr_b16 v[118:119], v108
	s_waitcnt lgkmcnt(0)
	s_nop 0
	v_mfma_f32_16x16x32_bf16 v[0:3], v[0:3], v[116:119], v[4:7]
	s_nop 5
	v_lshl_add_u64 v[4:5], v[54:55], 2, s[22:23]
	s_nop 0
	global_store_dword v[60:61], v0, off offset:448
	global_store_dword v[4:5], v1, off offset:512
	global_store_dword v[4:5], v2, off offset:1024
	global_store_dword v[4:5], v3, off offset:1536
	s_and_saveexec_b64 s[24:25], s[18:19]
	s_cbranch_execz .LBB0_965
; #define LAS __attribute__((address_space(3)))
; template <int NW> DI void ml1_unit(const Params& P, const Frame& F, int cidx) {
;     ...
;     if (F.tid < 128) { float s = 0.f; for (int j = 0; j < 64; ++j) s += bf2f(*(const LAS bf16*)(KWs + j * 272 + F.tid * 2)); DCT[128 * 128 + F.tid] = s; }
	ds_read_u16 v0, v113 offset:17408
	ds_read_u16 v1, v113 offset:17680
	s_waitcnt lgkmcnt(1)
	v_lshlrev_b32_e32 v0, 16, v0
	v_add_f32_e32 v0, 0, v0
	s_waitcnt lgkmcnt(0)
	v_lshlrev_b32_e32 v1, 16, v1
	v_add_f32_e32 v0, v0, v1
	ds_read_u16 v1, v113 offset:17952
	s_waitcnt lgkmcnt(0)
	v_lshlrev_b32_e32 v1, 16, v1
	v_add_f32_e32 v0, v0, v1
	ds_read_u16 v1, v113 offset:18224
	s_waitcnt lgkmcnt(0)
	v_lshlrev_b32_e32 v1, 16, v1
	v_add_f32_e32 v0, v0, v1
	ds_read_u16 v1, v113 offset:18496
	s_waitcnt lgkmcnt(0)
	v_lshlrev_b32_e32 v1, 16, v1
	v_add_f32_e32 v0, v0, v1
	ds_read_u16 v1, v113 offset:18768
	s_waitcnt lgkmcnt(0)
	v_lshlrev_b32_e32 v1, 16, v1
	v_add_f32_e32 v0, v0, v1
	ds_read_u16 v1, v113 offset:19040
	s_waitcnt lgkmcnt(0)
	v_lshlrev_b32_e32 v1, 16, v1
	v_add_f32_e32 v0, v0, v1
	ds_read_u16 v1, v113 offset:19312
	s_waitcnt lgkmcnt(0)
	v_lshlrev_b32_e32 v1, 16, v1
	v_add_f32_e32 v0, v0, v1
	ds_read_u16 v1, v113 offset:19584
	s_waitcnt lgkmcnt(0)
	v_lshlrev_b32_e32 v1, 16, v1
	v_add_f32_e32 v0, v0, v1
	ds_read_u16 v1, v113 offset:19856
	s_waitcnt lgkmcnt(0)
	v_lshlrev_b32_e32 v1, 16, v1
	v_add_f32_e32 v0, v0, v1
	ds_read_u16 v1, v113 offset:20128
	s_waitcnt lgkmcnt(0)
	v_lshlrev_b32_e32 v1, 16, v1
	v_add_f32_e32 v0, v0, v1
	ds_read_u16 v1, v113 offset:20400
	s_waitcnt lgkmcnt(0)
	v_lshlrev_b32_e32 v1, 16, v1
	v_add_f32_e32 v0, v0, v1
	ds_read_u16 v1, v113 offset:20672
	s_waitcnt lgkmcnt(0)
	v_lshlrev_b32_e32 v1, 16, v1
	v_add_f32_e32 v0, v0, v1
	ds_read_u16 v1, v113 offset:20944
	s_waitcnt lgkmcnt(0)
	v_lshlrev_b32_e32 v1, 16, v1
	v_add_f32_e32 v0, v0, v1
	ds_read_u16 v1, v113 offset:21216
	s_waitcnt lgkmcnt(0)
	v_lshlrev_b32_e32 v1, 16, v1
	v_add_f32_e32 v0, v0, v1
	ds_read_u16 v1, v113 offset:21488
	s_waitcnt lgkmcnt(0)
	v_lshlrev_b32_e32 v1, 16, v1
	v_add_f32_e32 v0, v0, v1
	ds_read_u16 v1, v113 offset:21760
	s_waitcnt lgkmcnt(0)
	v_lshlrev_b32_e32 v1, 16, v1
	v_add_f32_e32 v0, v0, v1
	ds_read_u16 v1, v113 offset:22032
	s_waitcnt lgkmcnt(0)
	v_lshlrev_b32_e32 v1, 16, v1
	v_add_f32_e32 v0, v0, v1
	ds_read_u16 v1, v113 offset:22304
	s_waitcnt lgkmcnt(0)
	v_lshlrev_b32_e32 v1, 16, v1
	v_add_f32_e32 v0, v0, v1
	ds_read_u16 v1, v113 offset:22576
	s_waitcnt lgkmcnt(0)
	v_lshlrev_b32_e32 v1, 16, v1
	v_add_f32_e32 v0, v0, v1
	ds_read_u16 v1, v113 offset:22848
	s_waitcnt lgkmcnt(0)
	v_lshlrev_b32_e32 v1, 16, v1
	v_add_f32_e32 v0, v0, v1
	ds_read_u16 v1, v113 offset:23120
	s_waitcnt lgkmcnt(0)
	v_lshlrev_b32_e32 v1, 16, v1
	v_add_f32_e32 v0, v0, v1
	ds_read_u16 v1, v113 offset:23392
	s_waitcnt lgkmcnt(0)
	v_lshlrev_b32_e32 v1, 16, v1
	v_add_f32_e32 v0, v0, v1
	ds_read_u16 v1, v113 offset:23664
	s_waitcnt lgkmcnt(0)
	v_lshlrev_b32_e32 v1, 16, v1
	v_add_f32_e32 v0, v0, v1
	ds_read_u16 v1, v113 offset:23936
	s_waitcnt lgkmcnt(0)
	v_lshlrev_b32_e32 v1, 16, v1
	v_add_f32_e32 v0, v0, v1
	ds_read_u16 v1, v113 offset:24208
	s_waitcnt lgkmcnt(0)
	v_lshlrev_b32_e32 v1, 16, v1
	v_add_f32_e32 v0, v0, v1
	ds_read_u16 v1, v113 offset:24480
	s_waitcnt lgkmcnt(0)
	v_lshlrev_b32_e32 v1, 16, v1
	v_add_f32_e32 v0, v0, v1
	ds_read_u16 v1, v113 offset:24752
	s_waitcnt lgkmcnt(0)
	v_lshlrev_b32_e32 v1, 16, v1
	v_add_f32_e32 v0, v0, v1
	ds_read_u16 v1, v113 offset:25024
	s_waitcnt lgkmcnt(0)
	v_lshlrev_b32_e32 v1, 16, v1
	v_add_f32_e32 v0, v0, v1
	ds_read_u16 v1, v113 offset:25296
	s_waitcnt lgkmcnt(0)
	v_lshlrev_b32_e32 v1, 16, v1
	v_add_f32_e32 v0, v0, v1
	ds_read_u16 v1, v113 offset:25568
	s_waitcnt lgkmcnt(0)
	v_lshlrev_b32_e32 v1, 16, v1
	v_add_f32_e32 v0, v0, v1
	ds_read_u16 v1, v113 offset:25840
	s_waitcnt lgkmcnt(0)
	v_lshlrev_b32_e32 v1, 16, v1
	v_add_f32_e32 v0, v0, v1
	ds_read_u16 v1, v113 offset:26112
	s_waitcnt lgkmcnt(0)
; #define LAS __attribute__((address_space(3)))
; template <int NW> DI void ml1_unit(const Params& P, const Frame& F, int cidx) {
;     ...
;     if (F.tid < 128) { float s = 0.f; for (int j = 0; j < 64; ++j) s += bf2f(*(const LAS bf16*)(KWs + j * 272 + F.tid * 2)); DCT[128 * 128 + F.tid] = s; }
	v_lshlrev_b32_e32 v1, 16, v1
	v_add_f32_e32 v0, v0, v1
	ds_read_u16 v1, v113 offset:26384
	s_waitcnt lgkmcnt(0)
	v_lshlrev_b32_e32 v1, 16, v1
	v_add_f32_e32 v0, v0, v1
	ds_read_u16 v1, v113 offset:26656
	s_waitcnt lgkmcnt(0)
	v_lshlrev_b32_e32 v1, 16, v1
	v_add_f32_e32 v0, v0, v1
	ds_read_u16 v1, v113 offset:26928
	s_waitcnt lgkmcnt(0)
	v_lshlrev_b32_e32 v1, 16, v1
	v_add_f32_e32 v0, v0, v1
	ds_read_u16 v1, v113 offset:27200
	s_waitcnt lgkmcnt(0)
	v_lshlrev_b32_e32 v1, 16, v1
	v_add_f32_e32 v0, v0, v1
	ds_read_u16 v1, v113 offset:27472
	s_waitcnt lgkmcnt(0)
	v_lshlrev_b32_e32 v1, 16, v1
	v_add_f32_e32 v0, v0, v1
	ds_read_u16 v1, v113 offset:27744
	s_waitcnt lgkmcnt(0)
	v_lshlrev_b32_e32 v1, 16, v1
	v_add_f32_e32 v0, v0, v1
	ds_read_u16 v1, v113 offset:28016
	s_waitcnt lgkmcnt(0)
	v_lshlrev_b32_e32 v1, 16, v1
	v_add_f32_e32 v0, v0, v1
	ds_read_u16 v1, v113 offset:28288
	s_waitcnt lgkmcnt(0)
	v_lshlrev_b32_e32 v1, 16, v1
	v_add_f32_e32 v0, v0, v1
	ds_read_u16 v1, v113 offset:28560
	s_waitcnt lgkmcnt(0)
	v_lshlrev_b32_e32 v1, 16, v1
	v_add_f32_e32 v0, v0, v1
	ds_read_u16 v1, v113 offset:28832
	s_waitcnt lgkmcnt(0)
	v_lshlrev_b32_e32 v1, 16, v1
	v_add_f32_e32 v0, v0, v1
	ds_read_u16 v1, v113 offset:29104
	s_waitcnt lgkmcnt(0)
	v_lshlrev_b32_e32 v1, 16, v1
	v_add_f32_e32 v0, v0, v1
	ds_read_u16 v1, v113 offset:29376
	s_waitcnt lgkmcnt(0)
	v_lshlrev_b32_e32 v1, 16, v1
	v_add_f32_e32 v0, v0, v1
	ds_read_u16 v1, v113 offset:29648
	s_waitcnt lgkmcnt(0)
	v_lshlrev_b32_e32 v1, 16, v1
	v_add_f32_e32 v0, v0, v1
	ds_read_u16 v1, v113 offset:29920
	s_waitcnt lgkmcnt(0)
	v_lshlrev_b32_e32 v1, 16, v1
	v_add_f32_e32 v0, v0, v1
	ds_read_u16 v1, v113 offset:30192
	s_waitcnt lgkmcnt(0)
	v_lshlrev_b32_e32 v1, 16, v1
	v_add_f32_e32 v0, v0, v1
	ds_read_u16 v1, v113 offset:30464
	s_waitcnt lgkmcnt(0)
	v_lshlrev_b32_e32 v1, 16, v1
	v_add_f32_e32 v0, v0, v1
	ds_read_u16 v1, v113 offset:30736
	s_waitcnt lgkmcnt(0)
	v_lshlrev_b32_e32 v1, 16, v1
	v_add_f32_e32 v0, v0, v1
	ds_read_u16 v1, v113 offset:31008
	s_waitcnt lgkmcnt(0)
	v_lshlrev_b32_e32 v1, 16, v1
	v_add_f32_e32 v0, v0, v1
	ds_read_u16 v1, v113 offset:31280
	s_waitcnt lgkmcnt(0)
	v_lshlrev_b32_e32 v1, 16, v1
	v_add_f32_e32 v0, v0, v1
	ds_read_u16 v1, v113 offset:31552
	s_waitcnt lgkmcnt(0)
	v_lshlrev_b32_e32 v1, 16, v1
	v_add_f32_e32 v0, v0, v1
	ds_read_u16 v1, v113 offset:31824
	s_waitcnt lgkmcnt(0)
	v_lshlrev_b32_e32 v1, 16, v1
	v_add_f32_e32 v0, v0, v1
	ds_read_u16 v1, v113 offset:32096
	s_waitcnt lgkmcnt(0)
	v_lshlrev_b32_e32 v1, 16, v1
	v_add_f32_e32 v0, v0, v1
	ds_read_u16 v1, v113 offset:32368
	s_waitcnt lgkmcnt(0)
	v_lshlrev_b32_e32 v1, 16, v1
	v_add_f32_e32 v0, v0, v1
	ds_read_u16 v1, v113 offset:32640
	s_waitcnt lgkmcnt(0)
	v_lshlrev_b32_e32 v1, 16, v1
	v_add_f32_e32 v0, v0, v1
	ds_read_u16 v1, v113 offset:32912
	s_waitcnt lgkmcnt(0)
	v_lshlrev_b32_e32 v1, 16, v1
	v_add_f32_e32 v0, v0, v1
	ds_read_u16 v1, v113 offset:33184
	s_waitcnt lgkmcnt(0)
	v_lshlrev_b32_e32 v1, 16, v1
	v_add_f32_e32 v0, v0, v1
	ds_read_u16 v1, v113 offset:33456
	s_waitcnt lgkmcnt(0)
	v_lshlrev_b32_e32 v1, 16, v1
	v_add_f32_e32 v0, v0, v1
	ds_read_u16 v1, v113 offset:33728
	s_waitcnt lgkmcnt(0)
	v_lshlrev_b32_e32 v1, 16, v1
	v_add_f32_e32 v0, v0, v1
	ds_read_u16 v1, v113 offset:34000
	s_waitcnt lgkmcnt(0)
	v_lshlrev_b32_e32 v1, 16, v1
	v_add_f32_e32 v0, v0, v1
	ds_read_u16 v1, v113 offset:34272
	s_waitcnt lgkmcnt(0)
	v_lshlrev_b32_e32 v1, 16, v1
	v_add_f32_e32 v0, v0, v1
	ds_read_u16 v1, v113 offset:34544
	s_waitcnt lgkmcnt(0)
	v_lshlrev_b32_e32 v1, 16, v1
	v_add_f32_e32 v2, v0, v1
	v_lshl_add_u64 v[0:1], s[22:23], 0, v[10:11]
	v_add_co_u32_e32 v0, vcc, 0x10000, v0
	s_nop 1
	v_addc_co_u32_e32 v1, vcc, 0, v1, vcc
	global_store_dword v[0:1], v2, off
	s_branch .LBB0_965

.LBB0_1017:
	s_cmp_lt_u32 s3, 0x40001
	s_mov_b64 s[18:19], 0
	s_cselect_b64 s[20:21], -1, 0
	s_mov_b64 s[22:23], -1
	s_and_b64 vcc, exec, s[20:21]
	s_cbranch_vccnz .LBB0_1014
	s_branch .LBB0_1011
	s_nop 0
	s_nop 0
	s_nop 0
	s_nop 0
	s_nop 0
	s_nop 0
	s_nop 0
	s_nop 0
	s_nop 0
	s_nop 0
	s_nop 0
	s_nop 0
	s_nop 0
	s_nop 0
	s_nop 0
	s_nop 0
	s_nop 0
	s_nop 0
.LBB0_1018:
	s_or_b64 exec, exec, s[14:15]
	s_and_b64 s[14:15], s[16:17], exec

; #define LAS __attribute__((address_space(3)))
; DI unsigned pk2(float lo, float hi) { const f32x2 v = {lo, hi}; return __builtin_bit_cast(unsigned, __builtin_convertvector(v, bf16x2_t)); }
; template <int NW> DI void ml1_unit(const Params& P, const Frame& F, int cidx) {
;     ...
;     for (int id = F.tid; id < 2048; id += NT) { const int which = id >> 10, rem = id & 1023, row = rem >> 4, ch = rem & 15;
;         if (which == 0) *(LAS u32x4*)(Vs + row * 272 + ch * 16) = *(const u32x4*)(Z + (r0 + row) * NZ + 6144 + h * 128 + ch * 8);
;         else { const u32x4 k = *(const u32x4*)(ZC + (r0 + row) * 2560 + 2048 + h * 128 + ch * 8); const float w = wl[row];
;             u32x4 o; o.x = pk2(bflo(k.x) * w, bfhi(k.x) * w); o.y = pk2(bflo(k.y) * w, bfhi(k.y) * w); o.z = pk2(bflo(k.z) * w, bfhi(k.z) * w); o.w = pk2(bflo(k.w) * w, bfhi(k.w) * w);
;             *(LAS u32x4*)(KWs + row * 272 + ch * 16) = o; } }
.LBB0_2533:
	s_or_b64 exec, exec, s[22:23]
	s_lshl_b32 s0, s34, 8
	v_lshl_add_u64 v[0:1], v[16:17], 0, s[0:1]
	s_waitcnt lgkmcnt(0)
	s_barrier
	global_load_dwordx4 v[186:189], v[0:1], off
	v_lshl_add_u64 v[2:3], v[18:19], 0, s[0:1]
	global_load_dwordx4 v[190:193], v[2:3], off
	v_lshl_add_u64 v[0:1], v[20:21], 0, s[0:1]
	global_load_dwordx4 v[194:197], v[0:1], off
	v_lshl_add_u64 v[2:3], v[22:23], 0, s[0:1]
	global_load_dwordx4 v[198:201], v[2:3], off
	s_add_i32 s0, s33, s27
	s_and_b32 s0, s0, 3
	s_lshl_b32 s0, s0, 8
	s_xor_b64 s[22:23], s[24:25], -1
	v_lshl_add_u64 v[0:1], v[58:59], 0, s[0:1]
	global_load_dwordx4 v[202:205], v[0:1], off
	v_lshl_add_u64 v[0:1], v[0:1], 0, s[20:21]
	global_load_dwordx4 v[206:209], v[0:1], off
	v_lshl_add_u64 v[0:1], v[0:1], 0, s[20:21]
	global_load_dwordx4 v[210:213], v[0:1], off
	v_lshl_add_u64 v[0:1], v[0:1], 0, s[20:21]
	global_load_dwordx4 v[214:217], v[0:1], off
	ds_read_b32 v230, v69
	ds_read_b32 v232, v69 offset:64
	ds_read_b32 v234, v69 offset:128
	ds_read_b32 v236, v69 offset:192
	v_mad_u32_u24 v244, v56, s28, v114
	v_add_u32_e32 v3, 16, v56
	v_mad_u32_u24 v245, v3, s28, v114
	v_add_u32_e32 v3, 32, v56
	v_mad_u32_u24 v246, v3, s28, v114
	v_add_u32_e32 v3, 48, v56
	v_mad_u32_u24 v247, v3, s28, v114
	s_waitcnt vmcnt(7)
	ds_write_b128 v57, v[186:189]
	s_waitcnt vmcnt(6)
	ds_write_b128 v57, v[190:193] offset:4352
	s_waitcnt vmcnt(5)
	ds_write_b128 v57, v[194:197] offset:8704
	s_waitcnt vmcnt(4)
	ds_write_b128 v57, v[198:201] offset:13056
	s_waitcnt vmcnt(3)
	s_waitcnt lgkmcnt(4)
	v_lshlrev_b32_e32 v60, 16, v202
	v_and_b32_e32 v61, 0xffff0000, v202
	v_pk_mul_f32 v[60:61], v[230:231], v[60:61] op_sel_hi:[0,1]
	v_cvt_pk_bf16_f32 v202, v60, v61
	v_lshlrev_b32_e32 v60, 16, v203
	v_and_b32_e32 v61, 0xffff0000, v203
	v_pk_mul_f32 v[60:61], v[230:231], v[60:61] op_sel_hi:[0,1]
	v_cvt_pk_bf16_f32 v203, v60, v61
	v_lshlrev_b32_e32 v60, 16, v204
	v_and_b32_e32 v61, 0xffff0000, v204
	v_pk_mul_f32 v[60:61], v[230:231], v[60:61] op_sel_hi:[0,1]
	v_cvt_pk_bf16_f32 v204, v60, v61
	v_lshlrev_b32_e32 v60, 16, v205
	v_and_b32_e32 v61, 0xffff0000, v205
	v_pk_mul_f32 v[60:61], v[230:231], v[60:61] op_sel_hi:[0,1]
	v_cvt_pk_bf16_f32 v205, v60, v61
	ds_write_b128 v244, v[202:205] offset:17408
	s_waitcnt vmcnt(2)
	v_lshlrev_b32_e32 v60, 16, v206
	v_and_b32_e32 v61, 0xffff0000, v206
	v_pk_mul_f32 v[60:61], v[232:233], v[60:61] op_sel_hi:[0,1]
	v_cvt_pk_bf16_f32 v206, v60, v61
	v_lshlrev_b32_e32 v60, 16, v207
	v_and_b32_e32 v61, 0xffff0000, v207
	v_pk_mul_f32 v[60:61], v[232:233], v[60:61] op_sel_hi:[0,1]
	v_cvt_pk_bf16_f32 v207, v60, v61
	v_lshlrev_b32_e32 v60, 16, v208
	v_and_b32_e32 v61, 0xffff0000, v208
	v_pk_mul_f32 v[60:61], v[232:233], v[60:61] op_sel_hi:[0,1]
	v_cvt_pk_bf16_f32 v208, v60, v61
	v_lshlrev_b32_e32 v60, 16, v209
	v_and_b32_e32 v61, 0xffff0000, v209
	v_pk_mul_f32 v[60:61], v[232:233], v[60:61] op_sel_hi:[0,1]
	v_cvt_pk_bf16_f32 v209, v60, v61
	ds_write_b128 v245, v[206:209] offset:17408
	s_waitcnt vmcnt(1)
	v_lshlrev_b32_e32 v60, 16, v210
	v_and_b32_e32 v61, 0xffff0000, v210
	v_pk_mul_f32 v[60:61], v[234:235], v[60:61] op_sel_hi:[0,1]
	v_cvt_pk_bf16_f32 v210, v60, v61
	v_lshlrev_b32_e32 v60, 16, v211
	v_and_b32_e32 v61, 0xffff0000, v211
	v_pk_mul_f32 v[60:61], v[234:235], v[60:61] op_sel_hi:[0,1]
	v_cvt_pk_bf16_f32 v211, v60, v61
	v_lshlrev_b32_e32 v60, 16, v212
	v_and_b32_e32 v61, 0xffff0000, v212
	v_pk_mul_f32 v[60:61], v[234:235], v[60:61] op_sel_hi:[0,1]
	v_cvt_pk_bf16_f32 v212, v60, v61
	v_lshlrev_b32_e32 v60, 16, v213
	v_and_b32_e32 v61, 0xffff0000, v213
	v_pk_mul_f32 v[60:61], v[234:235], v[60:61] op_sel_hi:[0,1]
	v_cvt_pk_bf16_f32 v213, v60, v61
	ds_write_b128 v246, v[210:213] offset:17408
	s_waitcnt vmcnt(0)
	v_lshlrev_b32_e32 v60, 16, v214
	v_and_b32_e32 v61, 0xffff0000, v214
	v_pk_mul_f32 v[60:61], v[236:237], v[60:61] op_sel_hi:[0,1]
	v_cvt_pk_bf16_f32 v214, v60, v61
	v_lshlrev_b32_e32 v60, 16, v215
	v_and_b32_e32 v61, 0xffff0000, v215
	v_pk_mul_f32 v[60:61], v[236:237], v[60:61] op_sel_hi:[0,1]
	v_cvt_pk_bf16_f32 v215, v60, v61
	v_lshlrev_b32_e32 v60, 16, v216
	v_and_b32_e32 v61, 0xffff0000, v216
	v_pk_mul_f32 v[60:61], v[236:237], v[60:61] op_sel_hi:[0,1]
	v_cvt_pk_bf16_f32 v216, v60, v61
	v_lshlrev_b32_e32 v60, 16, v217
	v_and_b32_e32 v61, 0xffff0000, v217
	v_pk_mul_f32 v[60:61], v[236:237], v[60:61] op_sel_hi:[0,1]
	v_cvt_pk_bf16_f32 v217, v60, v61
	ds_write_b128 v247, v[214:217] offset:17408
	s_mov_b64 s[24:25], exec
	s_or_b64 exec, exec, s[24:25]
	s_waitcnt lgkmcnt(0)
	s_barrier
; DI bf16x8 frag_tr(unsigned base_addr, int RS, int k0, int c0, int lane) { const int g = lane >> 4; return frag_tr2(base_addr, RS, k0 + 8 * g, k0 + 8 * g + 4, c0, lane); }
; #define MFMA16(a, b, c) __builtin_amdgcn_mfma_f32_16x16x32_bf16((a), (b), (c), 0, 0, 0)
; template <int NW> DI void ml1_unit(const Params& P, const Frame& F, int cidx) {
;     ...
;     float* DCT = (float*)(ws + WS_T + T_DCT) + (size_t)cidx * 16512;
;     const unsigned Va = (unsigned)(size_t)Vs, Ka = (unsigned)(size_t)KWs;
; #pragma unroll
;     for (int mi = 0; mi < 8 / NW; ++mi) { const int mt = F.wave + NW * mi;
;         bf16x8 af[2];
; #pragma unroll
;         for (int ks = 0; ks < 2; ++ks) af[ks] = frag_tr(Va, 272, 32 * ks, 16 * mt, lane);
; #pragma unroll
;         for (int nt = 0; nt < 8; ++nt) { f32x4 a = (f32x4){0.f, 0.f, 0.f, 0.f};
; #pragma unroll
;             for (int ks = 0; ks < 2; ++ks) a = MFMA16(af[ks], frag_tr(Ka, 272, 32 * ks, 16 * nt, lane), a);
; #pragma unroll
;             for (int e = 0; e < 4; ++e) DCT[(16 * mt + 4 * rq + e) * 128 + 16 * nt + c] = a[e]; } }
	ds_read_b64_tr_b16 v[4:5], v70
	ds_read_b64_tr_b16 v[6:7], v71
	s_waitcnt lgkmcnt(0)
	ds_read_b64_tr_b16 v[0:1], v74
	ds_read_b64_tr_b16 v[2:3], v75
	s_waitcnt lgkmcnt(0)
	ds_read_b64_tr_b16 v[116:117], v76
	ds_read_b64_tr_b16 v[118:119], v78
	s_waitcnt lgkmcnt(0)
	s_lshl_b32 s0, s26, 5
	v_mfma_f32_16x16x32_bf16 v[116:119], v[4:7], v[116:119], 0
	s_or_b32 s0, s0, s3
	s_mul_hi_i32 s25, s0, 0x10200
	s_mul_i32 s0, s0, 0x10200
	ds_read_b64_tr_b16 v[120:121], v79
	ds_read_b64_tr_b16 v[122:123], v80
	s_waitcnt lgkmcnt(0)
	s_add_u32 s24, s29, s0
	v_mfma_f32_16x16x32_bf16 v[116:119], v[0:3], v[120:123], v[116:119]
	s_addc_u32 s25, s30, s25
	v_lshl_add_u64 v[60:61], v[14:15], 2, s[24:25]
	v_lshl_add_u64 v[124:125], v[26:27], 2, s[24:25]
	v_lshl_add_u64 v[126:127], v[30:31], 2, s[24:25]
	v_lshl_add_u64 v[128:129], v[32:33], 2, s[24:25]
	s_nop 2
	global_store_dword v[60:61], v116, off
	v_lshl_add_u64 v[60:61], v[24:25], 2, s[24:25]
	global_store_dword v[60:61], v117, off offset:512
	global_store_dword v[60:61], v118, off offset:1024
	global_store_dword v[60:61], v119, off offset:1536
	ds_read_b64_tr_b16 v[116:117], v81
	ds_read_b64_tr_b16 v[118:119], v82
	s_waitcnt lgkmcnt(0)
	ds_read_b64_tr_b16 v[120:121], v83
	ds_read_b64_tr_b16 v[122:123], v84
	s_waitcnt lgkmcnt(0)
	v_lshl_add_u64 v[130:131], v[36:37], 2, s[24:25]
	v_mfma_f32_16x16x32_bf16 v[116:119], v[4:7], v[116:119], 0
	v_lshl_add_u64 v[132:133], v[38:39], 2, s[24:25]
	v_lshl_add_u64 v[134:135], v[12:13], 2, s[24:25]
	v_lshl_add_u64 v[136:137], v[40:41], 2, s[24:25]
	v_mfma_f32_16x16x32_bf16 v[116:119], v[0:3], v[120:123], v[116:119]
	s_nop 7
	global_store_dword v[60:61], v116, off offset:64
	global_store_dword v[124:125], v117, off offset:512
	global_store_dword v[124:125], v118, off offset:1024
	global_store_dword v[124:125], v119, off offset:1536
	ds_read_b64_tr_b16 v[116:117], v85
	ds_read_b64_tr_b16 v[118:119], v86
	s_waitcnt lgkmcnt(0)
	ds_read_b64_tr_b16 v[120:121], v87
	ds_read_b64_tr_b16 v[122:123], v88
	s_waitcnt lgkmcnt(0)
	v_lshl_add_u64 v[124:125], v[28:29], 2, s[24:25]
	v_mfma_f32_16x16x32_bf16 v[116:119], v[4:7], v[116:119], 0
	v_lshl_add_u64 v[138:139], v[44:45], 2, s[24:25]
	v_lshl_add_u64 v[140:141], v[46:47], 2, s[24:25]
	v_lshl_add_u64 v[142:143], v[48:49], 2, s[24:25]
	v_mfma_f32_16x16x32_bf16 v[116:119], v[0:3], v[120:123], v[116:119]
	s_nop 7
	global_store_dword v[60:61], v116, off offset:128
	global_store_dword v[124:125], v117, off offset:512
	global_store_dword v[124:125], v118, off offset:1024
	global_store_dword v[124:125], v119, off offset:1536
	ds_read_b64_tr_b16 v[116:117], v89
	ds_read_b64_tr_b16 v[118:119], v90
	s_waitcnt lgkmcnt(0)
	ds_read_b64_tr_b16 v[120:121], v91
	ds_read_b64_tr_b16 v[122:123], v92
	s_waitcnt lgkmcnt(0)
	v_lshl_add_u64 v[124:125], v[34:35], 2, s[24:25]
	v_mfma_f32_16x16x32_bf16 v[116:119], v[4:7], v[116:119], 0
	v_lshl_add_u64 v[144:145], v[50:51], 2, s[24:25]
	v_lshl_add_u64 v[146:147], v[54:55], 2, s[24:25]
	v_mfma_f32_16x16x32_bf16 v[116:119], v[0:3], v[120:123], v[116:119]
	s_nop 7
	global_store_dword v[60:61], v116, off offset:192
	global_store_dword v[126:127], v117, off offset:512
	global_store_dword v[126:127], v118, off offset:1024
	global_store_dword v[126:127], v119, off offset:1536
	ds_read_b64_tr_b16 v[116:117], v93
	ds_read_b64_tr_b16 v[118:119], v94
	s_waitcnt lgkmcnt(0)
	ds_read_b64_tr_b16 v[120:121], v95
	ds_read_b64_tr_b16 v[122:123], v96
	s_waitcnt lgkmcnt(0)
	v_lshl_add_u64 v[126:127], v[42:43], 2, s[24:25]
	v_mfma_f32_16x16x32_bf16 v[116:119], v[4:7], v[116:119], 0
	v_mfma_f32_16x16x32_bf16 v[116:119], v[0:3], v[120:123], v[116:119]
	s_nop 7
	global_store_dword v[60:61], v116, off offset:256
	global_store_dword v[128:129], v117, off offset:512
	global_store_dword v[128:129], v118, off offset:1024
	global_store_dword v[128:129], v119, off offset:1536
	ds_read_b64_tr_b16 v[116:117], v97
	ds_read_b64_tr_b16 v[118:119], v98
	s_waitcnt lgkmcnt(0)
	ds_read_b64_tr_b16 v[120:121], v99
	ds_read_b64_tr_b16 v[122:123], v100
	s_waitcnt lgkmcnt(0)
	v_lshl_add_u64 v[128:129], v[52:53], 2, s[24:25]
	v_mfma_f32_16x16x32_bf16 v[116:119], v[4:7], v[116:119], 0
	v_mfma_f32_16x16x32_bf16 v[116:119], v[0:3], v[120:123], v[116:119]
	s_nop 7
	global_store_dword v[60:61], v116, off offset:320
	global_store_dword v[124:125], v117, off offset:512
	global_store_dword v[124:125], v118, off offset:1024
	global_store_dword v[124:125], v119, off offset:1536
	ds_read_b64_tr_b16 v[116:117], v101
	ds_read_b64_tr_b16 v[118:119], v102
	s_waitcnt lgkmcnt(0)
	ds_read_b64_tr_b16 v[120:121], v103
	ds_read_b64_tr_b16 v[122:123], v104
	s_waitcnt lgkmcnt(0)
	s_nop 0
	v_mfma_f32_16x16x32_bf16 v[116:119], v[4:7], v[116:119], 0
	v_mfma_f32_16x16x32_bf16 v[116:119], v[0:3], v[120:123], v[116:119]
	s_nop 7
	global_store_dword v[60:61], v116, off offset:384
	global_store_dword v[130:131], v117, off offset:512
	global_store_dword v[130:131], v118, off offset:1024
	global_store_dword v[130:131], v119, off offset:1536
	ds_read_b64_tr_b16 v[116:117], v105
	ds_read_b64_tr_b16 v[118:119], v106
	s_waitcnt lgkmcnt(0)
	s_nop 0
	v_mfma_f32_16x16x32_bf16 v[4:7], v[4:7], v[116:119], 0
	ds_read_b64_tr_b16 v[116:117], v107
	ds_read_b64_tr_b16 v[118:119], v108
	s_waitcnt lgkmcnt(0)
	s_nop 0
	v_mfma_f32_16x16x32_bf16 v[0:3], v[0:3], v[116:119], v[4:7]
	s_nop 7
	global_store_dword v[60:61], v0, off offset:448
	global_store_dword v[132:133], v1, off offset:512
	global_store_dword v[132:133], v2, off offset:1024
	global_store_dword v[132:133], v3, off offset:1536
	ds_read_b64_tr_b16 v[0:1], v109
	ds_read_b64_tr_b16 v[2:3], v110
	s_waitcnt lgkmcnt(0)
; DI bf16x8 frag_tr(unsigned base_addr, int RS, int k0, int c0, int lane) { const int g = lane >> 4; return frag_tr2(base_addr, RS, k0 + 8 * g, k0 + 8 * g + 4, c0, lane); }
; #define MFMA16(a, b, c) __builtin_amdgcn_mfma_f32_16x16x32_bf16((a), (b), (c), 0, 0, 0)
; template <int NW> DI void ml1_unit(const Params& P, const Frame& F, int cidx) {
;     ...
; #pragma unroll
;     for (int mi = 0; mi < 8 / NW; ++mi) { const int mt = F.wave + NW * mi;
;         bf16x8 af[2];
; #pragma unroll
;         for (int ks = 0; ks < 2; ++ks) af[ks] = frag_tr(Va, 272, 32 * ks, 16 * mt, lane);
; #pragma unroll
;         for (int nt = 0; nt < 8; ++nt) { f32x4 a = (f32x4){0.f, 0.f, 0.f, 0.f};
; #pragma unroll
;             for (int ks = 0; ks < 2; ++ks) a = MFMA16(af[ks], frag_tr(Ka, 272, 32 * ks, 16 * nt, lane), a);
; #pragma unroll
;             for (int e = 0; e < 4; ++e) DCT[(16 * mt + 4 * rq + e) * 128 + 16 * nt + c] = a[e]; } }
	ds_read_b64_tr_b16 v[4:5], v111
	ds_read_b64_tr_b16 v[6:7], v112
	s_waitcnt lgkmcnt(0)
	ds_read_b64_tr_b16 v[116:117], v76
	ds_read_b64_tr_b16 v[118:119], v78
	s_waitcnt lgkmcnt(0)
	ds_read_b64_tr_b16 v[120:121], v79
	ds_read_b64_tr_b16 v[122:123], v80
	s_waitcnt lgkmcnt(0)
	s_nop 0
	v_mfma_f32_16x16x32_bf16 v[116:119], v[0:3], v[116:119], 0
	v_mfma_f32_16x16x32_bf16 v[116:119], v[4:7], v[120:123], v[116:119]
	s_nop 7
	global_store_dword v[134:135], v116, off
	global_store_dword v[136:137], v117, off offset:512
	global_store_dword v[136:137], v118, off offset:1024
	global_store_dword v[136:137], v119, off offset:1536
	ds_read_b64_tr_b16 v[116:117], v81
	ds_read_b64_tr_b16 v[118:119], v82
	s_waitcnt lgkmcnt(0)
	ds_read_b64_tr_b16 v[120:121], v83
	ds_read_b64_tr_b16 v[122:123], v84
	s_waitcnt lgkmcnt(0)
	s_nop 0
	v_mfma_f32_16x16x32_bf16 v[116:119], v[0:3], v[116:119], 0
	v_mfma_f32_16x16x32_bf16 v[116:119], v[4:7], v[120:123], v[116:119]
	s_nop 7
	global_store_dword v[136:137], v116, off offset:64
	global_store_dword v[126:127], v117, off offset:512
	global_store_dword v[126:127], v118, off offset:1024
	global_store_dword v[126:127], v119, off offset:1536
	ds_read_b64_tr_b16 v[116:117], v85
	ds_read_b64_tr_b16 v[118:119], v86
	s_waitcnt lgkmcnt(0)
	ds_read_b64_tr_b16 v[120:121], v87
	ds_read_b64_tr_b16 v[122:123], v88
	s_waitcnt lgkmcnt(0)
	s_nop 0
	v_mfma_f32_16x16x32_bf16 v[116:119], v[0:3], v[116:119], 0
	v_mfma_f32_16x16x32_bf16 v[116:119], v[4:7], v[120:123], v[116:119]
	s_nop 7
	global_store_dword v[136:137], v116, off offset:128
	global_store_dword v[138:139], v117, off offset:512
	global_store_dword v[138:139], v118, off offset:1024
	global_store_dword v[138:139], v119, off offset:1536
	ds_read_b64_tr_b16 v[116:117], v89
	ds_read_b64_tr_b16 v[118:119], v90
	s_waitcnt lgkmcnt(0)
	ds_read_b64_tr_b16 v[120:121], v91
	ds_read_b64_tr_b16 v[122:123], v92
	s_waitcnt lgkmcnt(0)
	s_nop 0
	v_mfma_f32_16x16x32_bf16 v[116:119], v[0:3], v[116:119], 0
	v_mfma_f32_16x16x32_bf16 v[116:119], v[4:7], v[120:123], v[116:119]
	s_nop 7
	global_store_dword v[136:137], v116, off offset:192
	global_store_dword v[140:141], v117, off offset:512
	global_store_dword v[140:141], v118, off offset:1024
	global_store_dword v[140:141], v119, off offset:1536
	ds_read_b64_tr_b16 v[116:117], v93
	ds_read_b64_tr_b16 v[118:119], v94
	s_waitcnt lgkmcnt(0)
	ds_read_b64_tr_b16 v[120:121], v95
	ds_read_b64_tr_b16 v[122:123], v96
	s_waitcnt lgkmcnt(0)
	s_nop 0
	v_mfma_f32_16x16x32_bf16 v[116:119], v[0:3], v[116:119], 0
	v_mfma_f32_16x16x32_bf16 v[116:119], v[4:7], v[120:123], v[116:119]
	s_nop 7
	global_store_dword v[136:137], v116, off offset:256
	global_store_dword v[142:143], v117, off offset:512
	global_store_dword v[142:143], v118, off offset:1024
	global_store_dword v[142:143], v119, off offset:1536
	ds_read_b64_tr_b16 v[116:117], v97
	ds_read_b64_tr_b16 v[118:119], v98
	s_waitcnt lgkmcnt(0)
	ds_read_b64_tr_b16 v[120:121], v99
	ds_read_b64_tr_b16 v[122:123], v100
	s_waitcnt lgkmcnt(0)
	s_nop 0
	v_mfma_f32_16x16x32_bf16 v[116:119], v[0:3], v[116:119], 0
	v_mfma_f32_16x16x32_bf16 v[116:119], v[4:7], v[120:123], v[116:119]
	s_nop 7
	global_store_dword v[136:137], v116, off offset:320
	global_store_dword v[144:145], v117, off offset:512
	global_store_dword v[144:145], v118, off offset:1024
	global_store_dword v[144:145], v119, off offset:1536
	ds_read_b64_tr_b16 v[116:117], v101
	ds_read_b64_tr_b16 v[118:119], v102
	s_waitcnt lgkmcnt(0)
	ds_read_b64_tr_b16 v[120:121], v103
	ds_read_b64_tr_b16 v[122:123], v104
	s_waitcnt lgkmcnt(0)
	s_nop 0
	v_mfma_f32_16x16x32_bf16 v[116:119], v[0:3], v[116:119], 0
	v_mfma_f32_16x16x32_bf16 v[116:119], v[4:7], v[120:123], v[116:119]
	s_nop 7
	global_store_dword v[136:137], v116, off offset:384
	global_store_dword v[128:129], v117, off offset:512
	global_store_dword v[128:129], v118, off offset:1024
	global_store_dword v[128:129], v119, off offset:1536
	ds_read_b64_tr_b16 v[116:117], v105
	ds_read_b64_tr_b16 v[118:119], v106
	s_waitcnt lgkmcnt(0)
	s_nop 0
	v_mfma_f32_16x16x32_bf16 v[0:3], v[0:3], v[116:119], 0
	ds_read_b64_tr_b16 v[116:117], v107
	ds_read_b64_tr_b16 v[118:119], v108
	s_waitcnt lgkmcnt(0)
	s_nop 0
	v_mfma_f32_16x16x32_bf16 v[0:3], v[4:7], v[116:119], v[0:3]
	s_nop 7
	global_store_dword v[136:137], v0, off offset:448
	global_store_dword v[146:147], v1, off offset:512
	global_store_dword v[146:147], v2, off offset:1024
	global_store_dword v[146:147], v3, off offset:1536
	s_and_saveexec_b64 s[26:27], s[18:19]
	s_cbranch_execz .LBB0_2530
; #define LAS __attribute__((address_space(3)))
; template <int NW> DI void ml1_unit(const Params& P, const Frame& F, int cidx) {
;     ...
;     if (F.tid < 128) { float s = 0.f; for (int j = 0; j < 64; ++j) s += bf2f(*(const LAS bf16*)(KWs + j * 272 + F.tid * 2)); DCT[128 * 128 + F.tid] = s; }
	ds_read_u16 v0, v113 offset:17408
	ds_read_u16 v1, v113 offset:32912
	ds_read_u16 v2, v113 offset:33184
	ds_read_u16 v3, v113 offset:33456
	ds_read_u16 v4, v113 offset:33728
	ds_read_u16 v5, v113 offset:34000
	ds_read_u16 v6, v113 offset:34272
	ds_read_u16 v7, v113 offset:34544
	s_waitcnt lgkmcnt(7)
	v_lshlrev_b32_e32 v0, 16, v0
	ds_read_u16 v60, v113 offset:17680
	ds_read_u16 v61, v113 offset:17952
	ds_read_u16 v77, v113 offset:18224
	ds_read_u16 v115, v113 offset:18496
	ds_read_u16 v116, v113 offset:18768
	ds_read_u16 v117, v113 offset:19040
	ds_read_u16 v118, v113 offset:19312
	ds_read_u16 v119, v113 offset:19584
	v_add_f32_e32 v0, 0, v0
	s_waitcnt lgkmcnt(7)
	v_lshlrev_b32_e32 v60, 16, v60
	v_add_f32_e32 v0, v0, v60
	s_waitcnt lgkmcnt(6)
	v_lshlrev_b32_e32 v60, 16, v61
	v_add_f32_e32 v0, v0, v60
	s_waitcnt lgkmcnt(5)
	v_lshlrev_b32_e32 v60, 16, v77
	v_add_f32_e32 v0, v0, v60
	s_waitcnt lgkmcnt(4)
	v_lshlrev_b32_e32 v60, 16, v115
	v_add_f32_e32 v0, v0, v60
	s_waitcnt lgkmcnt(3)
	v_lshlrev_b32_e32 v60, 16, v116
	v_add_f32_e32 v0, v0, v60
	s_waitcnt lgkmcnt(2)
	v_lshlrev_b32_e32 v60, 16, v117
	v_add_f32_e32 v0, v0, v60
	s_waitcnt lgkmcnt(1)
	v_lshlrev_b32_e32 v60, 16, v118
	v_add_f32_e32 v0, v0, v60
	s_waitcnt lgkmcnt(0)
	v_lshlrev_b32_e32 v60, 16, v119
	v_add_f32_e32 v0, v0, v60
	ds_read_u16 v60, v113 offset:19856
	ds_read_u16 v61, v113 offset:20128
	ds_read_u16 v77, v113 offset:20400
	ds_read_u16 v115, v113 offset:20672
	ds_read_u16 v116, v113 offset:20944
	ds_read_u16 v117, v113 offset:21216
	ds_read_u16 v118, v113 offset:21488
	ds_read_u16 v119, v113 offset:21760
	s_waitcnt lgkmcnt(7)
	v_lshlrev_b32_e32 v60, 16, v60
	v_add_f32_e32 v0, v0, v60
	s_waitcnt lgkmcnt(6)
	v_lshlrev_b32_e32 v60, 16, v61
	v_add_f32_e32 v0, v0, v60
	s_waitcnt lgkmcnt(5)
	v_lshlrev_b32_e32 v60, 16, v77
	v_add_f32_e32 v0, v0, v60
	s_waitcnt lgkmcnt(4)
	v_lshlrev_b32_e32 v60, 16, v115
	v_add_f32_e32 v0, v0, v60
	s_waitcnt lgkmcnt(3)
	v_lshlrev_b32_e32 v60, 16, v116
	v_add_f32_e32 v0, v0, v60
	s_waitcnt lgkmcnt(2)
	v_lshlrev_b32_e32 v60, 16, v117
	v_add_f32_e32 v0, v0, v60
	s_waitcnt lgkmcnt(1)
	v_lshlrev_b32_e32 v60, 16, v118
	v_add_f32_e32 v0, v0, v60
	s_waitcnt lgkmcnt(0)
	v_lshlrev_b32_e32 v60, 16, v119
	v_add_f32_e32 v0, v0, v60
	ds_read_u16 v60, v113 offset:22032
	ds_read_u16 v61, v113 offset:22304
	ds_read_u16 v77, v113 offset:22576
	ds_read_u16 v115, v113 offset:22848
	ds_read_u16 v116, v113 offset:23120
	ds_read_u16 v117, v113 offset:23392
	ds_read_u16 v118, v113 offset:23664
	ds_read_u16 v119, v113 offset:23936
	s_waitcnt lgkmcnt(7)
	v_lshlrev_b32_e32 v60, 16, v60
	v_add_f32_e32 v0, v0, v60
	s_waitcnt lgkmcnt(6)
	v_lshlrev_b32_e32 v60, 16, v61
	v_add_f32_e32 v0, v0, v60
	s_waitcnt lgkmcnt(5)
	v_lshlrev_b32_e32 v60, 16, v77
	v_add_f32_e32 v0, v0, v60
	s_waitcnt lgkmcnt(4)
	v_lshlrev_b32_e32 v60, 16, v115
	v_add_f32_e32 v0, v0, v60
	s_waitcnt lgkmcnt(3)
	v_lshlrev_b32_e32 v60, 16, v116
	v_add_f32_e32 v0, v0, v60
	s_waitcnt lgkmcnt(2)
	v_lshlrev_b32_e32 v60, 16, v117
	v_add_f32_e32 v0, v0, v60
	s_waitcnt lgkmcnt(1)
	v_lshlrev_b32_e32 v60, 16, v118
	v_add_f32_e32 v0, v0, v60
	s_waitcnt lgkmcnt(0)
	v_lshlrev_b32_e32 v60, 16, v119
	v_add_f32_e32 v0, v0, v60
	ds_read_u16 v60, v113 offset:24208
	ds_read_u16 v61, v113 offset:24480
	ds_read_u16 v77, v113 offset:24752
	ds_read_u16 v115, v113 offset:25024
	ds_read_u16 v116, v113 offset:25296
	ds_read_u16 v117, v113 offset:25568
	ds_read_u16 v118, v113 offset:25840
	ds_read_u16 v119, v113 offset:26112
	s_waitcnt lgkmcnt(7)
	v_lshlrev_b32_e32 v60, 16, v60
	v_add_f32_e32 v0, v0, v60
	s_waitcnt lgkmcnt(6)
	v_lshlrev_b32_e32 v60, 16, v61
	v_add_f32_e32 v0, v0, v60
	s_waitcnt lgkmcnt(5)
	v_lshlrev_b32_e32 v60, 16, v77
	v_add_f32_e32 v0, v0, v60
	s_waitcnt lgkmcnt(4)
; #define LAS __attribute__((address_space(3)))
; template <int NW> DI void ml1_unit(const Params& P, const Frame& F, int cidx) {
;     ...
;     if (F.tid < 128) { float s = 0.f; for (int j = 0; j < 64; ++j) s += bf2f(*(const LAS bf16*)(KWs + j * 272 + F.tid * 2)); DCT[128 * 128 + F.tid] = s; }
	v_lshlrev_b32_e32 v60, 16, v115
	v_add_f32_e32 v0, v0, v60
	s_waitcnt lgkmcnt(3)
	v_lshlrev_b32_e32 v60, 16, v116
	v_add_f32_e32 v0, v0, v60
	s_waitcnt lgkmcnt(2)
	v_lshlrev_b32_e32 v60, 16, v117
	v_add_f32_e32 v0, v0, v60
	s_waitcnt lgkmcnt(1)
	v_lshlrev_b32_e32 v60, 16, v118
	v_add_f32_e32 v0, v0, v60
	s_waitcnt lgkmcnt(0)
	v_lshlrev_b32_e32 v60, 16, v119
	v_add_f32_e32 v0, v0, v60
	ds_read_u16 v60, v113 offset:26384
	ds_read_u16 v61, v113 offset:26656
	ds_read_u16 v77, v113 offset:26928
	ds_read_u16 v115, v113 offset:27200
	ds_read_u16 v116, v113 offset:27472
	ds_read_u16 v117, v113 offset:27744
	ds_read_u16 v118, v113 offset:28016
	ds_read_u16 v119, v113 offset:28288
	s_waitcnt lgkmcnt(7)
	v_lshlrev_b32_e32 v60, 16, v60
	v_add_f32_e32 v0, v0, v60
	s_waitcnt lgkmcnt(6)
	v_lshlrev_b32_e32 v60, 16, v61
	v_add_f32_e32 v0, v0, v60
	s_waitcnt lgkmcnt(5)
	v_lshlrev_b32_e32 v60, 16, v77
	v_add_f32_e32 v0, v0, v60
	s_waitcnt lgkmcnt(4)
	v_lshlrev_b32_e32 v60, 16, v115
	v_add_f32_e32 v0, v0, v60
	s_waitcnt lgkmcnt(3)
	v_lshlrev_b32_e32 v60, 16, v116
	v_add_f32_e32 v0, v0, v60
	s_waitcnt lgkmcnt(2)
	v_lshlrev_b32_e32 v60, 16, v117
	v_add_f32_e32 v0, v0, v60
	s_waitcnt lgkmcnt(1)
	v_lshlrev_b32_e32 v60, 16, v118
	v_add_f32_e32 v0, v0, v60
	s_waitcnt lgkmcnt(0)
	v_lshlrev_b32_e32 v60, 16, v119
	v_add_f32_e32 v0, v0, v60
	ds_read_u16 v60, v113 offset:28560
	ds_read_u16 v61, v113 offset:28832
	ds_read_u16 v77, v113 offset:29104
	ds_read_u16 v115, v113 offset:29376
	ds_read_u16 v116, v113 offset:29648
	ds_read_u16 v117, v113 offset:29920
	ds_read_u16 v118, v113 offset:30192
	ds_read_u16 v119, v113 offset:30464
	s_waitcnt lgkmcnt(7)
	v_lshlrev_b32_e32 v60, 16, v60
	v_add_f32_e32 v0, v0, v60
	s_waitcnt lgkmcnt(6)
	v_lshlrev_b32_e32 v60, 16, v61
	v_add_f32_e32 v0, v0, v60
	s_waitcnt lgkmcnt(5)
	v_lshlrev_b32_e32 v60, 16, v77
	v_add_f32_e32 v0, v0, v60
	s_waitcnt lgkmcnt(4)
	v_lshlrev_b32_e32 v60, 16, v115
	v_add_f32_e32 v0, v0, v60
	s_waitcnt lgkmcnt(3)
	v_lshlrev_b32_e32 v60, 16, v116
	v_add_f32_e32 v0, v0, v60
	s_waitcnt lgkmcnt(2)
	v_lshlrev_b32_e32 v60, 16, v117
	v_add_f32_e32 v0, v0, v60
	s_waitcnt lgkmcnt(1)
	v_lshlrev_b32_e32 v60, 16, v118
	v_add_f32_e32 v0, v0, v60
	s_waitcnt lgkmcnt(0)
	v_lshlrev_b32_e32 v60, 16, v119
	v_add_f32_e32 v0, v0, v60
	ds_read_u16 v60, v113 offset:30736
	ds_read_u16 v61, v113 offset:31008
	ds_read_u16 v77, v113 offset:31280
	ds_read_u16 v115, v113 offset:31552
	ds_read_u16 v116, v113 offset:31824
	ds_read_u16 v117, v113 offset:32096
	ds_read_u16 v118, v113 offset:32368
	ds_read_u16 v119, v113 offset:32640
	s_waitcnt lgkmcnt(7)
	v_lshlrev_b32_e32 v60, 16, v60
	v_add_f32_e32 v0, v0, v60
	s_waitcnt lgkmcnt(6)
	v_lshlrev_b32_e32 v60, 16, v61
	v_add_f32_e32 v0, v0, v60
	s_waitcnt lgkmcnt(5)
	v_lshlrev_b32_e32 v60, 16, v77
	v_add_f32_e32 v0, v0, v60
	s_waitcnt lgkmcnt(4)
	v_lshlrev_b32_e32 v60, 16, v115
	v_add_f32_e32 v0, v0, v60
	s_waitcnt lgkmcnt(3)
	v_lshlrev_b32_e32 v60, 16, v116
	v_add_f32_e32 v0, v0, v60
	s_waitcnt lgkmcnt(2)
	v_lshlrev_b32_e32 v60, 16, v117
	v_add_f32_e32 v0, v0, v60
	s_waitcnt lgkmcnt(1)
	v_lshlrev_b32_e32 v60, 16, v118
	v_add_f32_e32 v0, v0, v60
	s_waitcnt lgkmcnt(0)
	v_lshlrev_b32_e32 v60, 16, v119
	v_add_f32_e32 v0, v0, v60
	v_lshlrev_b32_e32 v1, 16, v1
	v_add_f32_e32 v0, v0, v1
	v_lshlrev_b32_e32 v1, 16, v2
	v_add_f32_e32 v0, v0, v1
	v_lshlrev_b32_e32 v1, 16, v3
	v_add_f32_e32 v0, v0, v1
	v_lshlrev_b32_e32 v1, 16, v4
	v_add_f32_e32 v0, v0, v1
	v_lshlrev_b32_e32 v1, 16, v5
	v_add_f32_e32 v0, v0, v1
	v_lshlrev_b32_e32 v1, 16, v6
	v_add_f32_e32 v0, v0, v1
	v_lshlrev_b32_e32 v1, 16, v7
	v_add_f32_e32 v2, v0, v1
	v_lshl_add_u64 v[0:1], s[24:25], 0, v[10:11]
	v_add_co_u32_e32 v0, vcc, 0x10000, v0
	s_nop 1
	v_addc_co_u32_e32 v1, vcc, 0, v1, vcc
	global_store_dword v[0:1], v2, off
	s_branch .LBB0_2530

.LBB0_2582:
	s_cmp_lt_u32 s3, 0x40001
	s_mov_b64 s[18:19], 0
	s_cselect_b64 s[20:21], -1, 0
	s_mov_b64 s[22:23], -1
	s_and_b64 vcc, exec, s[20:21]
	s_cbranch_vccnz .LBB0_2579
	s_branch .LBB0_2576
	s_nop 0
	s_nop 0
	s_nop 0
	s_nop 0
	s_nop 0
	s_nop 0
	s_nop 0
	s_nop 0
	s_nop 0
	s_nop 0
	s_nop 0
	s_nop 0
	s_nop 0
	s_nop 0
	s_nop 0
.LBB0_2583:
	s_or_b64 exec, exec, s[14:15]
	s_and_b64 s[14:15], s[16:17], exec
